# GDN chain loader: non-temporal (nt) loads for the once-read operand tiles
# speedup vs baseline: 1.0041x; 1.0041x over previous
; __device__ void phase_gdn_chain(const Params& p, int l, char* smem, int vb, int nvb, int oz) {
;     ...
;             GDN_LOAD(ra, va, ga, 0)
.LBB0_418:
	s_or_saveexec_b64 s[0:1], s[48:49]
	v_readlane_b32 s14, v254, 11
	v_readlane_b32 s4, v254, 1
	v_readlane_b32 s5, v254, 2
	v_readlane_b32 s6, v254, 3
	v_readlane_b32 s7, v254, 4
	v_readlane_b32 s8, v254, 5
	v_readlane_b32 s9, v254, 6
	v_readlane_b32 s10, v254, 7
	v_readlane_b32 s11, v254, 8
	v_readlane_b32 s12, v254, 9
	v_readlane_b32 s13, v254, 10
	v_readlane_b32 s15, v254, 12
	s_xor_b64 exec, exec, s[0:1]
	s_cbranch_execz .LBB0_389
	s_lshl_b32 s3, s46, 2
	s_or_b32 s2, s3, s2
	s_mul_i32 s2, s2, 36
	s_or_b32 s24, s2, s82
	s_ashr_i32 s25, s24, 31
	s_add_u32 s26, s24, s84
	s_addc_u32 s27, s25, 0
	s_lshl_b64 s[42:43], s[26:27], 13
	s_add_u32 s46, s4, s42
	s_addc_u32 s47, s5, s43
	s_add_u32 s48, s6, s42
	s_addc_u32 s49, s7, s43
	s_lshl_b64 s[24:25], s[24:25], 13
	s_add_u32 s50, s8, s24
	s_addc_u32 s51, s9, s25
	s_add_u32 s24, s10, s24
	s_addc_u32 s25, s11, s25
	s_add_u32 s42, s12, s42
	v_lshlrev_b32_e32 v2, 1, v202
	s_addc_u32 s43, s13, s43
	v_lshlrev_b32_e32 v215, 1, v204
	global_load_dwordx4 v[148:151], v2, s[46:47] nt
	global_load_dwordx4 v[152:155], v2, s[48:49] nt
	global_load_dwordx4 v[156:159], v215, s[48:49] nt
	global_load_dwordx4 v[160:163], v215, s[50:51] nt
	global_load_dwordx4 v[168:171], v2, s[50:51] nt
	global_load_dwordx4 v[164:167], v2, s[24:25] nt
	global_load_dwordx4 v[184:187], v215, s[46:47] nt
	global_load_dwordx4 v[172:175], v2, s[42:43] nt
	global_load_dwordx4 v[180:183], v215, s[24:25] nt
	global_load_dwordx4 v[176:179], v215, s[42:43] nt
	s_lshl_b64 s[24:25], s[26:27], 10
	s_add_u32 s42, s14, s24
	s_addc_u32 s43, s15, s25
	v_mov_b32_e32 v217, 0
	v_lshlrev_b32_e32 v216, 2, v190
	v_mov_b32_e32 v218, 0
	s_and_saveexec_b64 s[46:47], s[38:39]
	s_cbranch_execz .LBB0_421
	global_load_dword v218, v216, s[42:43]

; __device__ void phase_gdn_chain(const Params& p, int l, char* smem, int vb, int nvb, int oz) {
;     ...
;             GDN_LOAD(rb, vb_, gb, 1)
.LBB0_423:
	s_or_b64 exec, exec, s[46:47]
	s_or_b32 s24, s2, s83
	s_ashr_i32 s25, s24, 31
	s_add_u32 s26, s24, s84
	s_addc_u32 s27, s25, 0
	s_lshl_b64 s[42:43], s[26:27], 13
	s_add_u32 s46, s4, s42
	s_addc_u32 s47, s5, s43
	s_add_u32 s48, s6, s42
	s_addc_u32 s49, s7, s43
	s_lshl_b64 s[24:25], s[24:25], 13
	s_add_u32 s50, s8, s24
	s_addc_u32 s51, s9, s25
	s_add_u32 s24, s10, s24
	s_addc_u32 s25, s11, s25
	s_add_u32 s42, s12, s42
	s_addc_u32 s43, s13, s43
	global_load_dwordx4 v[68:71], v2, s[46:47] nt
	global_load_dwordx4 v[72:75], v2, s[48:49] nt
	global_load_dwordx4 v[76:79], v215, s[48:49] nt
	global_load_dwordx4 v[80:83], v215, s[50:51] nt
	global_load_dwordx4 v[88:91], v2, s[50:51] nt
	global_load_dwordx4 v[84:87], v2, s[24:25] nt
	global_load_dwordx4 v[96:99], v215, s[46:47] nt
	global_load_dwordx4 v[92:95], v2, s[42:43] nt
	global_load_dwordx4 v[104:107], v215, s[24:25] nt
	global_load_dwordx4 v[100:103], v215, s[42:43] nt
	s_lshl_b64 s[24:25], s[26:27], 10
	s_add_u32 s42, s14, s24
	s_addc_u32 s43, s15, s25
	v_mov_b32_e32 v219, 0
	v_mov_b32_e32 v220, 0
	s_and_saveexec_b64 s[46:47], s[38:39]
	s_cbranch_execz .LBB0_425
	global_load_dword v220, v216, s[42:43]

; __device__ void phase_gdn_chain(const Params& p, int l, char* smem, int vb, int nvb, int oz) {
;     ...
;             GDN_LOAD(rc, vc_, gc, 2)
.LBB0_427:
	s_or_b64 exec, exec, s[46:47]
	s_sub_i32 s3, s2, s80
	s_add_i32 s24, s3, 2
	s_ashr_i32 s25, s24, 31
	s_add_u32 s26, s24, s84
	s_addc_u32 s27, s25, 0
	s_lshl_b64 s[42:43], s[26:27], 13
	s_add_u32 s46, s4, s42
	s_addc_u32 s47, s5, s43
	s_add_u32 s48, s6, s42
	s_addc_u32 s49, s7, s43
	s_lshl_b64 s[24:25], s[24:25], 13
	s_add_u32 s50, s8, s24
	s_addc_u32 s51, s9, s25
	s_add_u32 s24, s10, s24
	s_addc_u32 s25, s11, s25
	s_add_u32 s42, s12, s42
	s_addc_u32 s43, s13, s43
	global_load_dwordx4 v[108:111], v2, s[46:47] nt
	global_load_dwordx4 v[112:115], v2, s[48:49] nt
	global_load_dwordx4 v[116:119], v215, s[48:49] nt
	global_load_dwordx4 v[120:123], v215, s[50:51] nt
	global_load_dwordx4 v[124:127], v2, s[50:51] nt
	global_load_dwordx4 v[128:131], v2, s[24:25] nt
	global_load_dwordx4 v[136:139], v215, s[46:47] nt
	global_load_dwordx4 v[132:135], v2, s[42:43] nt
	global_load_dwordx4 v[140:143], v215, s[24:25] nt
	global_load_dwordx4 v[144:147], v215, s[42:43] nt
	s_lshl_b64 s[24:25], s[26:27], 10
	s_add_u32 s42, s14, s24
	s_addc_u32 s43, s15, s25
	v_mov_b32_e32 v221, 0
	v_mov_b32_e32 v222, 0
	s_and_saveexec_b64 s[46:47], s[38:39]
	s_cbranch_execz .LBB0_429
	global_load_dword v222, v216, s[42:43]

; __device__ void phase_gdn_chain(const Params& p, int l, char* smem, int vb, int nvb, int oz) {
;     ...
;             GDN_LOAD(ra, va, ga, 0)
;             GDN_LOAD(rb, vb_, gb, 1)
;             GDN_LOAD(rc, vc_, gc, 2)
;             GDN_FILL(ra, va, ga, 0)
;             GDN_LOAD(ra, va, ga, 3)
.LBB0_431:
	s_or_b64 exec, exec, s[46:47]
	v_add_u32_e32 v223, 0, v211
	s_waitcnt vmcnt(20)
	ds_write_b128 v223, v[148:151]
	ds_write_b128 v223, v[184:187] offset:4608
	ds_write_b128 v223, v[152:155] offset:9216
	ds_write_b128 v223, v[156:159] offset:13824
	ds_write_b128 v223, v[168:171] offset:18432
	ds_write_b128 v223, v[160:163] offset:23040
	ds_write_b128 v223, v[164:167] offset:27648
	ds_write_b128 v223, v[180:183] offset:32256
	ds_write_b128 v193, v[172:175] offset:36864
	ds_write_b128 v193, v[176:179] offset:40960
	s_and_saveexec_b64 s[42:43], s[38:39]
	ds_write_b32 v213, v218 offset:45056
	s_or_b64 exec, exec, s[42:43]
	s_and_saveexec_b64 s[42:43], s[40:41]
	ds_write_b32 v3, v217 offset:45568
	s_or_b64 exec, exec, s[42:43]
	s_or_b32 s24, s2, s85
	s_ashr_i32 s25, s24, 31
	s_add_u32 s26, s24, s84
	s_addc_u32 s27, s25, 0
	s_lshl_b64 s[42:43], s[26:27], 13
	s_add_u32 s46, s4, s42
	s_addc_u32 s47, s5, s43
	s_add_u32 s48, s6, s42
	s_addc_u32 s49, s7, s43
	s_lshl_b64 s[24:25], s[24:25], 13
	s_add_u32 s50, s8, s24
	s_addc_u32 s51, s9, s25
	s_add_u32 s24, s10, s24
	s_addc_u32 s25, s11, s25
	s_add_u32 s42, s12, s42
	s_addc_u32 s43, s13, s43
	global_load_dwordx4 v[148:151], v2, s[46:47] nt
	global_load_dwordx4 v[152:155], v2, s[48:49] nt
	global_load_dwordx4 v[156:159], v215, s[48:49] nt
	global_load_dwordx4 v[160:163], v215, s[50:51] nt
	global_load_dwordx4 v[164:167], v2, s[50:51] nt
	global_load_dwordx4 v[168:171], v2, s[24:25] nt
	global_load_dwordx4 v[172:175], v215, s[46:47] nt
	global_load_dwordx4 v[176:179], v2, s[42:43] nt
	global_load_dwordx4 v[180:183], v215, s[24:25] nt
	global_load_dwordx4 v[184:187], v215, s[42:43] nt
	s_lshl_b64 s[24:25], s[26:27], 10
	s_add_u32 s42, s14, s24
	s_addc_u32 s43, s15, s25
	s_and_saveexec_b64 s[46:47], s[38:39]
	s_cbranch_execz .LBB0_437
	global_load_dword v218, v216, s[42:43]

; #define LDS_BARRIER() asm volatile("s_waitcnt lgkmcnt(0)\n\ts_barrier" ::: "memory")
; __device__ void phase_gdn_chain(const Params& p, int l, char* smem, int vb, int nvb, int oz) {
;     ...
;             for (int ci = 0; ci < 36; ci += 6) {
;                 GDN_FILL(rb, vb_, gb, 1)  if (ci + 4 < 36) GDN_LOAD(rb, vb_, gb, ci + 4)  LDS_BARRIER();
;                 GDN_FILL(rc, vc_, gc, 0)  if (ci + 5 < 36) GDN_LOAD(rc, vc_, gc, ci + 5)  LDS_BARRIER();
;                 GDN_FILL(ra, va, ga, 1)  if (ci + 6 < 36) GDN_LOAD(ra, va, ga, ci + 6)  LDS_BARRIER();
;                 GDN_FILL(rb, vb_, gb, 0)  if (ci + 7 < 36) GDN_LOAD(rb, vb_, gb, ci + 7)  LDS_BARRIER();
;                 GDN_FILL(rc, vc_, gc, 1)  if (ci + 8 < 36) GDN_LOAD(rc, vc_, gc, ci + 8)  LDS_BARRIER();
;                 if (ci + 6 < 36) GDN_FILL(ra, va, ga, 0)  if (ci + 9 < 36) GDN_LOAD(ra, va, ga, ci + 9)  LDS_BARRIER();
.LBB0_446:
	s_or_b64 exec, exec, s[42:43]
	s_add_i32 s25, s3, -5
	s_add_i32 s31, s24, 5
	s_and_b64 s[26:27], s[44:45], exec
	s_cselect_b32 s25, s25, s31
	s_add_i32 s26, s25, s2
	s_ashr_i32 s27, s26, 31
	s_add_u32 s42, s26, s84
	s_addc_u32 s43, s27, 0
	s_lshl_b64 s[46:47], s[42:43], 13
	s_add_u32 s48, s4, s46
	s_addc_u32 s49, s5, s47
	s_add_u32 s50, s6, s46
	s_addc_u32 s51, s7, s47
	s_lshl_b64 s[26:27], s[26:27], 13
	s_add_u32 s52, s8, s26
	s_addc_u32 s53, s9, s27
	s_add_u32 s26, s10, s26
	s_addc_u32 s27, s11, s27
	s_add_u32 s46, s12, s46
	s_addc_u32 s47, s13, s47
	global_load_dwordx4 v[68:71], v2, s[48:49] nt
	global_load_dwordx4 v[72:75], v2, s[50:51] nt
	global_load_dwordx4 v[76:79], v215, s[50:51] nt
	global_load_dwordx4 v[80:83], v215, s[52:53] nt
	global_load_dwordx4 v[88:91], v2, s[52:53] nt
	global_load_dwordx4 v[84:87], v2, s[26:27] nt
	global_load_dwordx4 v[96:99], v215, s[48:49] nt
	global_load_dwordx4 v[92:95], v2, s[46:47] nt
	global_load_dwordx4 v[104:107], v215, s[26:27] nt
	global_load_dwordx4 v[100:103], v215, s[46:47] nt
	s_lshl_b64 s[26:27], s[42:43], 10
	s_add_u32 s42, s14, s26
	s_addc_u32 s43, s15, s27
	s_and_saveexec_b64 s[46:47], s[38:39]
	s_cbranch_execz .LBB0_448
	global_load_dword v220, v216, s[42:43]

; #define LDS_BARRIER() asm volatile("s_waitcnt lgkmcnt(0)\n\ts_barrier" ::: "memory")
; __device__ void phase_gdn_chain(const Params& p, int l, char* smem, int vb, int nvb, int oz) {
;     ...
;             for (int ci = 0; ci < 36; ci += 6) {
;                 GDN_FILL(rb, vb_, gb, 1)  if (ci + 4 < 36) GDN_LOAD(rb, vb_, gb, ci + 4)  LDS_BARRIER();
;                 GDN_FILL(rc, vc_, gc, 0)  if (ci + 5 < 36) GDN_LOAD(rc, vc_, gc, ci + 5)  LDS_BARRIER();
;                 GDN_FILL(ra, va, ga, 1)  if (ci + 6 < 36) GDN_LOAD(ra, va, ga, ci + 6)  LDS_BARRIER();
;                 GDN_FILL(rb, vb_, gb, 0)  if (ci + 7 < 36) GDN_LOAD(rb, vb_, gb, ci + 7)  LDS_BARRIER();
;                 GDN_FILL(rc, vc_, gc, 1)  if (ci + 8 < 36) GDN_LOAD(rc, vc_, gc, ci + 8)  LDS_BARRIER();
;                 if (ci + 6 < 36) GDN_FILL(ra, va, ga, 0)  if (ci + 9 < 36) GDN_LOAD(ra, va, ga, ci + 9)  LDS_BARRIER();
.LBB0_450:
	s_or_b64 exec, exec, s[46:47]
	s_waitcnt lgkmcnt(0)
	s_barrier
	s_waitcnt vmcnt(20)
	ds_write_b128 v223, v[108:111]
	ds_write_b128 v223, v[136:139] offset:4608
	ds_write_b128 v223, v[112:115] offset:9216
	ds_write_b128 v223, v[116:119] offset:13824
	ds_write_b128 v223, v[124:127] offset:18432
	ds_write_b128 v223, v[120:123] offset:23040
	ds_write_b128 v223, v[128:131] offset:27648
	ds_write_b128 v223, v[140:143] offset:32256
	ds_write_b128 v193, v[132:135] offset:36864
	ds_write_b128 v193, v[144:147] offset:40960
	s_and_saveexec_b64 s[42:43], s[38:39]
	ds_write_b32 v213, v222 offset:45056
	s_or_b64 exec, exec, s[42:43]
	s_and_saveexec_b64 s[42:43], s[40:41]
	ds_write_b32 v3, v221 offset:45568
	s_or_b64 exec, exec, s[42:43]
	s_add_i32 s25, s3, -4
	s_add_i32 s31, s24, 4
	s_and_b64 s[26:27], s[44:45], exec
	s_cselect_b32 s25, s25, s31
	s_add_i32 s26, s25, s2
	s_ashr_i32 s27, s26, 31
	s_add_u32 s42, s26, s84
	s_addc_u32 s43, s27, 0
	s_lshl_b64 s[46:47], s[42:43], 13
	s_add_u32 s48, s4, s46
	s_addc_u32 s49, s5, s47
	s_add_u32 s50, s6, s46
	s_addc_u32 s51, s7, s47
	s_lshl_b64 s[26:27], s[26:27], 13
	s_add_u32 s52, s8, s26
	s_addc_u32 s53, s9, s27
	s_add_u32 s26, s10, s26
	s_addc_u32 s27, s11, s27
	s_add_u32 s46, s12, s46
	s_addc_u32 s47, s13, s47
	global_load_dwordx4 v[108:111], v2, s[48:49] nt
	global_load_dwordx4 v[112:115], v2, s[50:51] nt
	global_load_dwordx4 v[116:119], v215, s[50:51] nt
	global_load_dwordx4 v[120:123], v215, s[52:53] nt
	global_load_dwordx4 v[124:127], v2, s[52:53] nt
	global_load_dwordx4 v[128:131], v2, s[26:27] nt
	global_load_dwordx4 v[136:139], v215, s[48:49] nt
	global_load_dwordx4 v[132:135], v2, s[46:47] nt
	global_load_dwordx4 v[140:143], v215, s[26:27] nt
	global_load_dwordx4 v[144:147], v215, s[46:47] nt
	s_lshl_b64 s[26:27], s[42:43], 10
	s_add_u32 s42, s14, s26
	s_addc_u32 s43, s15, s27
	s_and_saveexec_b64 s[46:47], s[38:39]
	s_cbranch_execz .LBB0_456
	global_load_dword v222, v216, s[42:43]

; #define LDS_BARRIER() asm volatile("s_waitcnt lgkmcnt(0)\n\ts_barrier" ::: "memory")
; __device__ void phase_gdn_chain(const Params& p, int l, char* smem, int vb, int nvb, int oz) {
;     ...
;             for (int ci = 0; ci < 36; ci += 6) {
;                 GDN_FILL(rb, vb_, gb, 1)  if (ci + 4 < 36) GDN_LOAD(rb, vb_, gb, ci + 4)  LDS_BARRIER();
;                 GDN_FILL(rc, vc_, gc, 0)  if (ci + 5 < 36) GDN_LOAD(rc, vc_, gc, ci + 5)  LDS_BARRIER();
;                 GDN_FILL(ra, va, ga, 1)  if (ci + 6 < 36) GDN_LOAD(ra, va, ga, ci + 6)  LDS_BARRIER();
;                 GDN_FILL(rb, vb_, gb, 0)  if (ci + 7 < 36) GDN_LOAD(rb, vb_, gb, ci + 7)  LDS_BARRIER();
;                 GDN_FILL(rc, vc_, gc, 1)  if (ci + 8 < 36) GDN_LOAD(rc, vc_, gc, ci + 8)  LDS_BARRIER();
;                 if (ci + 6 < 36) GDN_FILL(ra, va, ga, 0)  if (ci + 9 < 36) GDN_LOAD(ra, va, ga, ci + 9)  LDS_BARRIER();
.LBB0_462:
	s_or_b64 exec, exec, s[42:43]
	s_add_i32 s25, s3, -9
	s_cmp_lt_u32 s25, 30
	s_cselect_b64 s[42:43], -1, 0
	s_cmp_gt_u32 s25, 29
	s_cbranch_scc1 .LBB0_468
	s_add_i32 s31, s3, -3
	s_add_i32 s46, s24, 3
	s_and_b64 s[26:27], s[44:45], exec
	s_cselect_b32 s26, s31, s46
	s_add_i32 s26, s26, s2
	s_ashr_i32 s27, s26, 31
	s_add_u32 s46, s26, s84
	s_addc_u32 s47, s27, 0
	s_lshl_b64 s[48:49], s[46:47], 13
	s_add_u32 s50, s4, s48
	s_addc_u32 s51, s5, s49
	s_add_u32 s52, s6, s48
	s_addc_u32 s53, s7, s49
	s_lshl_b64 s[26:27], s[26:27], 13
	s_add_u32 s54, s8, s26
	s_addc_u32 s55, s9, s27
	s_add_u32 s26, s10, s26
	s_addc_u32 s27, s11, s27
	s_add_u32 s48, s12, s48
	s_addc_u32 s49, s13, s49
	global_load_dwordx4 v[148:151], v2, s[50:51] nt
	global_load_dwordx4 v[152:155], v2, s[52:53] nt
	global_load_dwordx4 v[156:159], v215, s[52:53] nt
	global_load_dwordx4 v[160:163], v215, s[54:55] nt
	global_load_dwordx4 v[164:167], v2, s[54:55] nt
	global_load_dwordx4 v[168:171], v2, s[26:27] nt
	global_load_dwordx4 v[172:175], v215, s[50:51] nt
	global_load_dwordx4 v[176:179], v2, s[48:49] nt
	global_load_dwordx4 v[180:183], v215, s[26:27] nt
	global_load_dwordx4 v[184:187], v215, s[48:49] nt
	s_lshl_b64 s[26:27], s[46:47], 10
	s_add_u32 s46, s14, s26
	s_addc_u32 s47, s15, s27
	s_and_saveexec_b64 s[48:49], s[38:39]
	s_cbranch_execz .LBB0_465
	global_load_dword v218, v216, s[46:47]

; #define LDS_BARRIER() asm volatile("s_waitcnt lgkmcnt(0)\n\ts_barrier" ::: "memory")
; __device__ void phase_gdn_chain(const Params& p, int l, char* smem, int vb, int nvb, int oz) {
;     ...
;             for (int ci = 0; ci < 36; ci += 6) {
;                 GDN_FILL(rb, vb_, gb, 1)  if (ci + 4 < 36) GDN_LOAD(rb, vb_, gb, ci + 4)  LDS_BARRIER();
;                 GDN_FILL(rc, vc_, gc, 0)  if (ci + 5 < 36) GDN_LOAD(rc, vc_, gc, ci + 5)  LDS_BARRIER();
;                 GDN_FILL(ra, va, ga, 1)  if (ci + 6 < 36) GDN_LOAD(ra, va, ga, ci + 6)  LDS_BARRIER();
;                 GDN_FILL(rb, vb_, gb, 0)  if (ci + 7 < 36) GDN_LOAD(rb, vb_, gb, ci + 7)  LDS_BARRIER();
;                 GDN_FILL(rc, vc_, gc, 1)  if (ci + 8 < 36) GDN_LOAD(rc, vc_, gc, ci + 8)  LDS_BARRIER();
;                 if (ci + 6 < 36) GDN_FILL(ra, va, ga, 0)  if (ci + 9 < 36) GDN_LOAD(ra, va, ga, ci + 9)  LDS_BARRIER();
.LBB0_473:
	s_add_i32 s31, s3, -2
	s_add_i32 s46, s24, 2
	s_and_b64 s[26:27], s[44:45], exec
	s_cselect_b32 s26, s31, s46
	s_add_i32 s26, s26, s2
	s_ashr_i32 s27, s26, 31
	s_add_u32 s46, s26, s84
	s_addc_u32 s47, s27, 0
	s_lshl_b64 s[48:49], s[46:47], 13
	s_add_u32 s50, s4, s48
	s_addc_u32 s51, s5, s49
	s_add_u32 s52, s6, s48
	s_addc_u32 s53, s7, s49
	s_lshl_b64 s[26:27], s[26:27], 13
	s_add_u32 s54, s8, s26
	s_addc_u32 s55, s9, s27
	s_add_u32 s26, s10, s26
	s_addc_u32 s27, s11, s27
	s_add_u32 s48, s12, s48
	s_addc_u32 s49, s13, s49
	global_load_dwordx4 v[68:71], v2, s[50:51] nt
	global_load_dwordx4 v[72:75], v2, s[52:53] nt
	global_load_dwordx4 v[76:79], v215, s[52:53] nt
	global_load_dwordx4 v[80:83], v215, s[54:55] nt
	global_load_dwordx4 v[88:91], v2, s[54:55] nt
	global_load_dwordx4 v[84:87], v2, s[26:27] nt
	global_load_dwordx4 v[96:99], v215, s[50:51] nt
	global_load_dwordx4 v[92:95], v2, s[48:49] nt
	global_load_dwordx4 v[104:107], v215, s[26:27] nt
	global_load_dwordx4 v[100:103], v215, s[48:49] nt
	s_lshl_b64 s[26:27], s[46:47], 10
	s_add_u32 s46, s14, s26
	s_addc_u32 s47, s15, s27
	s_and_saveexec_b64 s[48:49], s[38:39]
	s_cbranch_execz .LBB0_475
	global_load_dword v220, v216, s[46:47]

; #define LDS_BARRIER() asm volatile("s_waitcnt lgkmcnt(0)\n\ts_barrier" ::: "memory")
; __device__ void phase_gdn_chain(const Params& p, int l, char* smem, int vb, int nvb, int oz) {
;     ...
;             for (int ci = 0; ci < 36; ci += 6) {
;                 GDN_FILL(rb, vb_, gb, 1)  if (ci + 4 < 36) GDN_LOAD(rb, vb_, gb, ci + 4)  LDS_BARRIER();
;                 GDN_FILL(rc, vc_, gc, 0)  if (ci + 5 < 36) GDN_LOAD(rc, vc_, gc, ci + 5)  LDS_BARRIER();
;                 GDN_FILL(ra, va, ga, 1)  if (ci + 6 < 36) GDN_LOAD(ra, va, ga, ci + 6)  LDS_BARRIER();
;                 GDN_FILL(rb, vb_, gb, 0)  if (ci + 7 < 36) GDN_LOAD(rb, vb_, gb, ci + 7)  LDS_BARRIER();
;                 GDN_FILL(rc, vc_, gc, 1)  if (ci + 8 < 36) GDN_LOAD(rc, vc_, gc, ci + 8)  LDS_BARRIER();
;                 if (ci + 6 < 36) GDN_FILL(ra, va, ga, 0)  if (ci + 9 < 36) GDN_LOAD(ra, va, ga, ci + 9)  LDS_BARRIER();
.LBB0_483:
	s_add_i32 s31, s3, -1
	s_add_i32 s46, s24, 1
	s_and_b64 s[26:27], s[44:45], exec
	s_cselect_b32 s26, s31, s46
	s_add_i32 s26, s26, s2
	s_ashr_i32 s27, s26, 31
	s_add_u32 s46, s26, s84
	s_addc_u32 s47, s27, 0
	s_lshl_b64 s[48:49], s[46:47], 13
	s_add_u32 s50, s4, s48
	s_addc_u32 s51, s5, s49
	s_add_u32 s52, s6, s48
	s_addc_u32 s53, s7, s49
	s_lshl_b64 s[26:27], s[26:27], 13
	s_add_u32 s54, s8, s26
	s_addc_u32 s55, s9, s27
	s_add_u32 s26, s10, s26
	s_addc_u32 s27, s11, s27
	s_add_u32 s48, s12, s48
	s_addc_u32 s49, s13, s49
	global_load_dwordx4 v[108:111], v2, s[50:51] nt
	global_load_dwordx4 v[112:115], v2, s[52:53] nt
	global_load_dwordx4 v[116:119], v215, s[52:53] nt
	global_load_dwordx4 v[120:123], v215, s[54:55] nt
	global_load_dwordx4 v[124:127], v2, s[54:55] nt
	global_load_dwordx4 v[128:131], v2, s[26:27] nt
	global_load_dwordx4 v[136:139], v215, s[50:51] nt
	global_load_dwordx4 v[132:135], v2, s[48:49] nt
	global_load_dwordx4 v[140:143], v215, s[26:27] nt
	global_load_dwordx4 v[144:147], v215, s[48:49] nt
	s_lshl_b64 s[26:27], s[46:47], 10
	s_add_u32 s46, s14, s26
	s_addc_u32 s47, s15, s27
	s_and_saveexec_b64 s[48:49], s[38:39]
	s_cbranch_execz .LBB0_485
	global_load_dword v222, v216, s[46:47]

; #define LDS_BARRIER() asm volatile("s_waitcnt lgkmcnt(0)\n\ts_barrier" ::: "memory")
; __device__ void phase_gdn_chain(const Params& p, int l, char* smem, int vb, int nvb, int oz) {
;     ...
;             for (int ci = 0; ci < 36; ci += 6) {
;                 GDN_FILL(rb, vb_, gb, 1)  if (ci + 4 < 36) GDN_LOAD(rb, vb_, gb, ci + 4)  LDS_BARRIER();
;                 GDN_FILL(rc, vc_, gc, 0)  if (ci + 5 < 36) GDN_LOAD(rc, vc_, gc, ci + 5)  LDS_BARRIER();
;                 GDN_FILL(ra, va, ga, 1)  if (ci + 6 < 36) GDN_LOAD(ra, va, ga, ci + 6)  LDS_BARRIER();
;                 GDN_FILL(rb, vb_, gb, 0)  if (ci + 7 < 36) GDN_LOAD(rb, vb_, gb, ci + 7)  LDS_BARRIER();
;                 GDN_FILL(rc, vc_, gc, 1)  if (ci + 8 < 36) GDN_LOAD(rc, vc_, gc, ci + 8)  LDS_BARRIER();
;                 if (ci + 6 < 36) GDN_FILL(ra, va, ga, 0)  if (ci + 9 < 36) GDN_LOAD(ra, va, ga, ci + 9)  LDS_BARRIER();
.LBB0_494:
	s_cmp_gt_u32 s25, 26
	s_cbranch_scc1 .LBB0_499
	s_and_b64 s[26:27], s[44:45], exec
	s_cselect_b32 s26, s3, s24
	s_add_i32 s26, s26, s2
	s_ashr_i32 s27, s26, 31
	s_add_u32 s42, s26, s84
	s_addc_u32 s43, s27, 0
	s_lshl_b64 s[46:47], s[42:43], 13
	v_readlane_b32 s4, v254, 1
	s_add_u32 s48, s4, s46
	v_readlane_b32 s5, v254, 2
	s_addc_u32 s49, s5, s47
	v_readlane_b32 s6, v254, 3
	s_add_u32 s50, s6, s46
	v_readlane_b32 s7, v254, 4
	s_addc_u32 s51, s7, s47
	s_lshl_b64 s[26:27], s[26:27], 13
	v_readlane_b32 s8, v254, 5
	s_add_u32 s52, s8, s26
	v_readlane_b32 s9, v254, 6
	s_addc_u32 s53, s9, s27
	v_readlane_b32 s10, v254, 7
	s_add_u32 s26, s10, s26
	v_readlane_b32 s11, v254, 8
	s_addc_u32 s27, s11, s27
	v_readlane_b32 s12, v254, 9
	s_add_u32 s46, s12, s46
	v_readlane_b32 s13, v254, 10
	s_addc_u32 s47, s13, s47
	global_load_dwordx4 v[148:151], v2, s[48:49] nt
	global_load_dwordx4 v[152:155], v2, s[50:51] nt
	global_load_dwordx4 v[156:159], v215, s[50:51] nt
	global_load_dwordx4 v[160:163], v215, s[52:53] nt
	global_load_dwordx4 v[164:167], v2, s[52:53] nt
	global_load_dwordx4 v[168:171], v2, s[26:27] nt
	global_load_dwordx4 v[172:175], v215, s[48:49] nt
	global_load_dwordx4 v[176:179], v2, s[46:47] nt
	global_load_dwordx4 v[180:183], v215, s[26:27] nt
	global_load_dwordx4 v[184:187], v215, s[46:47] nt
	s_lshl_b64 s[26:27], s[42:43], 10
	v_readlane_b32 s14, v254, 11
	v_readlane_b32 s15, v254, 12
	s_add_u32 s42, s14, s26
	s_addc_u32 s43, s15, s27
	s_and_saveexec_b64 s[46:47], s[38:39]
	s_cbranch_execz .LBB0_497
	global_load_dword v218, v216, s[42:43]
